# speedup vs baseline: 1.0040x; 1.0040x over previous
.LBB1_6:
	s_and_b32 s16, s2, 7
	s_mul_i32 s0, s16, 0x4b
	s_add_i32 s22, s3, s0
	s_lshr_b32 s23, s25, 6
	s_cmp_ge_u32 s23, s14
	s_cselect_b64 s[0:1], -1, 0
	s_cmp_lt_u32 s23, s15
	s_cselect_b64 s[2:3], -1, 0
	s_and_b64 s[8:9], s[0:1], s[2:3]
	s_mul_i32 s2, s22, 0x28000
	s_movk_i32 s0, 0xc0
	s_mul_hi_u32 s1, s22, 0x28000
	s_waitcnt lgkmcnt(0)
	s_add_u32 s2, s4, s2
	v_lshlrev_b32_e32 v1, 2, v0
	s_addc_u32 s3, s5, s1
	v_add_u32_e32 v2, 0x500, v1
	v_cmp_gt_u32_e64 s[0:1], s0, v0
	v_lshlrev_b32_e32 v104, 4, v0
	s_mul_i32 s16, s16, 5
	v_cndmask_b32_e64 v1, v1, v2, s[0:1]
	v_lshlrev_b32_e32 v2, 2, v1
	global_load_dwordx4 v[68:71], v104, s[2:3] nt
	s_and_saveexec_b64 s[44:45], s[0:1]
	global_load_dwordx4 v[64:67], v2, s[2:3] nt
	s_mov_b64 exec, s[44:45]
	s_add_i32 s24, s23, s16
	v_mov_b32_e32 v105, 0
	s_mul_i32 s4, s24, 20
	s_mov_b32 s5, 0
	v_mov_b32_e32 v3, v105
	v_lshrrev_b32_e32 v1, 4, v0
	s_lshl_b64 s[14:15], s[4:5], 12
	v_lshlrev_b32_e32 v6, 3, v0
	v_lshl_add_u64 v[96:97], s[2:3], 0, v[104:105]
	v_lshl_add_u64 v[98:99], s[2:3], 0, v[2:3]
	s_add_u32 s2, s6, s14
	v_and_b32_e32 v104, 0x3f0, v104
	s_addc_u32 s3, s7, s15
	v_lshl_add_u64 v[2:3], s[2:3], 0, v[104:105]
	s_mov_b64 s[14:15], 0x32000
	s_mov_b32 s4, 0x32000
	v_lshl_add_u64 v[100:101], v[2:3], 0, s[14:15]
	v_add_co_u32_e32 v2, vcc, s4, v2
	s_nop 1
	v_addc_co_u32_e32 v3, vcc, 0, v3, vcc
	s_and_saveexec_b64 s[44:45], s[8:9]
	global_load_dwordx4 v[92:95], v[2:3], off
	global_load_dwordx4 v[80:83], v[100:101], off offset:1024
	global_load_dwordx4 v[88:91], v[100:101], off offset:2048
	global_load_dwordx4 v[84:87], v[100:101], off offset:3072
	s_mov_b64 exec, s[44:45]
	s_movk_i32 s4, 0x2000
	v_add_co_u32_e32 v2, vcc, s4, v96
	s_nop 1
	v_addc_co_u32_e32 v3, vcc, 0, v97, vcc
	v_add_co_u32_e32 v4, vcc, s4, v98
	s_nop 1
	v_addc_co_u32_e32 v5, vcc, 0, v99, vcc
	global_load_dwordx4 v[76:79], v[2:3], off nt
	s_and_saveexec_b64 s[44:45], s[0:1]
	global_load_dwordx4 v[72:75], v[4:5], off nt
	s_mov_b64 exec, s[44:45]
	v_bfe_u32 v2, v0, 2, 4
	v_and_b32_e32 v0, 63, v0
	v_mul_u32_u24_e32 v2, 0xa0, v2
	v_lshlrev_b32_e32 v104, 4, v0
	v_and_or_b32 v108, v6, 24, v2
	v_mul_u32_u24_e32 v2, 0xa0, v1
	v_and_b32_e32 v3, 0x78, v6
	v_lshl_add_u64 v[0:1], s[2:3], 0, v[104:105]
	s_mov_b64 s[2:3], 0x33c00
	v_mov_b32_e32 v60, v105
	v_mov_b32_e32 v61, v105
	v_lshl_add_u64 v[102:103], v[0:1], 0, s[2:3]
	v_mov_b32_e32 v104, v105
	v_mov_b32_e32 v62, v105
	v_mov_b32_e32 v63, v105
	v_add_u32_e32 v109, v2, v3
	v_mov_b64_e32 v[56:57], v[60:61]
	v_mov_b64_e32 v[52:53], v[60:61]
	v_mov_b64_e32 v[48:49], v[60:61]
	v_mov_b64_e32 v[44:45], v[60:61]
	v_mov_b64_e32 v[40:41], v[60:61]
	v_mov_b64_e32 v[36:37], v[60:61]
	v_mov_b64_e32 v[32:33], v[60:61]
	v_mov_b64_e32 v[28:29], v[60:61]
	v_mov_b64_e32 v[24:25], v[60:61]
	v_mov_b64_e32 v[20:21], v[60:61]
	v_mov_b64_e32 v[16:17], v[60:61]
	v_mov_b64_e32 v[12:13], v[60:61]
	v_mov_b64_e32 v[8:9], v[60:61]
	v_mov_b64_e32 v[4:5], v[60:61]
	v_mov_b64_e32 v[0:1], v[60:61]
	s_mov_b64 s[14:15], 0x2000
	v_mov_b64_e32 v[58:59], v[62:63]
	v_mov_b64_e32 v[54:55], v[62:63]
	v_mov_b64_e32 v[50:51], v[62:63]
	v_mov_b64_e32 v[46:47], v[62:63]
	v_mov_b64_e32 v[42:43], v[62:63]
	v_mov_b64_e32 v[38:39], v[62:63]
	v_mov_b64_e32 v[34:35], v[62:63]
	v_mov_b64_e32 v[30:31], v[62:63]
	v_mov_b64_e32 v[26:27], v[62:63]
	v_mov_b64_e32 v[22:23], v[62:63]
	v_mov_b64_e32 v[18:19], v[62:63]
	v_mov_b64_e32 v[14:15], v[62:63]
	v_mov_b64_e32 v[10:11], v[62:63]
	v_mov_b64_e32 v[6:7], v[62:63]
	v_mov_b64_e32 v[2:3], v[62:63]
	s_mov_b32 s26, 0
	v_mov_b64_e32 v[106:107], v[104:105]

.LBB1_14:
	ds_read_b64_tr_b16 v[66:67], v108 offset:2560
	ds_read_b64_tr_b16 v[64:65], v108
	ds_read_b64_tr_b16 v[68:69], v108 offset:32
	ds_read_b64_tr_b16 v[110:111], v108 offset:64
	ds_read_b64_tr_b16 v[114:115], v108 offset:96
	ds_read_b64_tr_b16 v[70:71], v108 offset:2592
	ds_read_b64_tr_b16 v[112:113], v108 offset:2624
	ds_read_b64_tr_b16 v[116:117], v108 offset:2656
	s_waitcnt vmcnt(5) lgkmcnt(6)
	v_mfma_f32_16x16x32_f16 v[60:63], v[64:67], v[92:95], v[60:63]
	s_mov_b64 s[16:17], -1
	s_and_b64 vcc, exec, s[10:11]
	s_waitcnt vmcnt(4)
	v_mfma_f32_16x16x32_f16 v[56:59], v[64:67], v[80:83], v[56:59]
	s_waitcnt vmcnt(3)
	v_mfma_f32_16x16x32_f16 v[52:55], v[64:67], v[88:91], v[52:55]
	s_waitcnt vmcnt(2)
	v_mfma_f32_16x16x32_f16 v[48:51], v[64:67], v[84:87], v[48:51]
	s_waitcnt lgkmcnt(2)
	v_mfma_f32_16x16x32_f16 v[44:47], v[68:71], v[92:95], v[44:47]
	v_mfma_f32_16x16x32_f16 v[40:43], v[68:71], v[80:83], v[40:43]
	v_mfma_f32_16x16x32_f16 v[36:39], v[68:71], v[88:91], v[36:39]
	v_mfma_f32_16x16x32_f16 v[32:35], v[68:71], v[84:87], v[32:35]
	s_waitcnt lgkmcnt(1)
	v_mfma_f32_16x16x32_f16 v[28:31], v[110:113], v[92:95], v[28:31]
	v_mfma_f32_16x16x32_f16 v[24:27], v[110:113], v[80:83], v[24:27]
	v_mfma_f32_16x16x32_f16 v[20:23], v[110:113], v[88:91], v[20:23]
	v_mfma_f32_16x16x32_f16 v[16:19], v[110:113], v[84:87], v[16:19]
	s_waitcnt lgkmcnt(0)
	v_mfma_f32_16x16x32_f16 v[12:15], v[114:117], v[92:95], v[12:15]
	v_mfma_f32_16x16x32_f16 v[8:11], v[114:117], v[80:83], v[8:11]
	v_mfma_f32_16x16x32_f16 v[4:7], v[114:117], v[88:91], v[4:7]
	v_mfma_f32_16x16x32_f16 v[0:3], v[114:117], v[84:87], v[0:3]
	s_cbranch_vccz .LBB1_16
	s_setprio 0
	s_mov_b64 s[16:17], 0
